# s16p + attention inner loop back edge rotated: loop-back barrier is the loop head, exit test and loop-carried moves in front of it, exit path has its own barrier copy (L0 and L1); padded
# speedup vs baseline: 1.0036x; 1.0036x over previous
; DI unsigned pk2(float lo, float hi) { const f32x2 v = {lo, hi}; return __builtin_bit_cast(unsigned, __builtin_convertvector(v, bf16x2_t)); }
; DI void attn_block(const Params& P, const Frame& F, int L, int b, int h, int qb, float lam, float oml) {
;     ...
;     const int q0 = qb * 128, qrow = q0 + 16 * wave + c;
;     const size_t rowbase = (size_t)b * SEQ;
;     bf16x8 qf[2][2];
; #pragma unroll
;     for (int j = 0; j < 2; ++j)
; #pragma unroll
;         for (int ks = 0; ks < 2; ++ks) qf[j][ks] = *(const bf16x8*)(Z + (rowbase + qrow) * NZ + 3072 + h * 128 + j * 64 + 32 * ks + 8 * rq);
;     const float LOG2E = 1.4426950408889634f;
;     const float sc = 0.125f * LOG2E, sl = __builtin_bit_cast(float, __builtin_amdgcn_readfirstlane(__builtin_bit_cast(int, exp2f(-(float)(h + 1)) * LOG2E)));
; #pragma unroll
;     for (int j = 0; j < 2; ++j)
; #pragma unroll
;         for (int ks = 0; ks < 2; ++ks) { const u32x4 qv = __builtin_bit_cast(u32x4, qf[j][ks]); u32x4 o;
;             o.x = pk2(bflo(qv.x) * sc, bfhi(qv.x) * sc); o.y = pk2(bflo(qv.y) * sc, bfhi(qv.y) * sc); o.z = pk2(bflo(qv.z) * sc, bfhi(qv.z) * sc); o.w = pk2(bflo(qv.w) * sc, bfhi(qv.w) * sc);
;             qf[j][ks] = __builtin_bit_cast(bf16x8, o); }
;     float sbias[16];
; #pragma unroll
;     for (int i = 0; i < 16; ++i) sbias[i] = __builtin_bit_cast(float, __builtin_amdgcn_readfirstlane(__builtin_bit_cast(int, sl * (float)(16 * (i >> 2) + (i & 3)))));
;     f32x4 O[2][8];
; #pragma unroll
;     for (int j = 0; j < 2; ++j)
; #pragma unroll
;         for (int d = 0; d < 8; ++d) O[j][d] = (f32x4){0.f, 0.f, 0.f, 0.f};
;     float mrun[2] = {-INFINITY, -INFINITY}, lrun[2] = {0.f, 0.f};
;     const int nkt = 2 * (qb + 1);
;     u32x4 st[4];
;     ...
;     ATT_LOAD(nkt - 1); ATT_STORE(0); __syncthreads();
; template <int L> DI void layer_phases(const Params& P, Frame& F, const XcdBarrier& bar, int lo, int hi) {
;     ...
;                 if (F.tid == 0) F.MISC[24] = __hip_atomic_fetch_add(qctr, 1u, __ATOMIC_RELAXED, __HIP_MEMORY_SCOPE_AGENT);
;                 __syncthreads();
;                 const int u = (int)F.MISC[24];
;                 if (u >= 1024) break;
;                 const int bh = u & 63; attn_block(P, F, L, bh >> 3, bh & 7, 15 - (u >> 6), lam, 1.0f - li); } }
.LBB0_1052:
	s_or_b64 exec, exec, s[6:7]
	v_mov_b32_e32 v0, s65
	s_waitcnt lgkmcnt(0)
	s_barrier
	ds_read_b32 v0, v0
	s_movk_i32 s6, 0x3ff
	s_waitcnt lgkmcnt(0)
	v_cmp_lt_i32_e32 vcc, s6, v0
	v_readfirstlane_b32 s11, v0
	s_mov_b64 s[6:7], -1
	s_cbranch_vccnz .LBB0_1047
	s_ashr_i32 s7, s11, 6
	s_sub_i32 s8, 15, s7
	s_lshl_b32 s9, s8, 7
	s_add_i32 s67, s9, s64
	s_lshl_b32 s6, s11, 8
	v_or_b32_e32 v0, s67, v127
	s_and_b32 s68, s6, 0x3800
	s_and_b32 s10, s11, 7
	v_add_u32_e32 v142, s68, v0
	v_mov_b64_e32 v[0:1], s[58:59]
	v_mad_u64_u32 v[2:3], s[12:13], v142, s3, v[0:1]
	s_lshl_b32 s38, s10, 8
	v_lshl_add_u64 v[2:3], v[2:3], 0, s[38:39]
	v_lshl_add_u64 v[2:3], v[124:125], 1, v[2:3]
	s_movk_i32 s6, 0x1000
	v_add_co_u32_e32 v4, vcc, s6, v2
	s_mov_b64 s[12:13], 0x1800
	s_nop 0
	v_addc_co_u32_e32 v5, vcc, 0, v3, vcc
	global_load_dwordx4 v[8:11], v[4:5], off offset:2048
	v_lshl_add_u64 v[2:3], v[2:3], 0, s[12:13]
	global_load_dwordx4 v[12:15], v[2:3], off offset:64
	global_load_dwordx4 v[24:27], v[2:3], off offset:128
	s_lshl_b32 s66, s10, 7
	s_add_i32 s10, s10, 1
	v_cvt_f32_ubyte0_e32 v4, s10
	s_mov_b32 s10, 0x42fc0000
	v_cmp_lt_f32_e32 vcc, s10, v4
	s_and_b64 s[12:13], vcc, exec
	s_cselect_b32 s12, 0xffffffc0, 0
	s_add_i32 s9, s68, s9
	s_mov_b32 s11, s39
	v_cndmask_b32_e32 v5, 0, v180, vcc
	global_load_dwordx4 v[28:31], v[2:3], off offset:192
	s_or_b32 s10, s9, 64
	v_sub_f32_e32 v4, v5, v4
	v_lshl_add_u64 v[2:3], s[10:11], 0, v[114:115]
	v_exp_f32_e32 v16, v4
	v_lshl_add_u64 v[4:5], s[10:11], 0, v[128:129]
	v_mad_u64_u32 v[6:7], s[10:11], v2, s3, v[0:1]
	v_mad_i32_i24 v7, v3, s3, v7
	v_lshlrev_b32_e32 v112, 1, v126
	v_mad_u64_u32 v[0:1], s[10:11], v4, s3, v[0:1]
	v_lshl_add_u64 v[2:3], v[6:7], 0, s[38:39]
	v_mad_i32_i24 v1, v5, s3, v1
	v_lshl_add_u64 v[2:3], v[2:3], 0, v[112:113]
	v_lshl_add_u64 v[0:1], v[0:1], 0, s[38:39]
	v_add_co_u32_e32 v4, vcc, s33, v2
	v_lshl_add_u64 v[0:1], v[0:1], 0, v[112:113]
	s_nop 0
	v_addc_co_u32_e32 v5, vcc, 0, v3, vcc
	v_add_co_u32_e32 v20, vcc, s33, v0
	v_ldexp_f32 v32, v16, s12
	s_nop 0
	v_addc_co_u32_e32 v21, vcc, 0, v1, vcc
	global_load_dwordx4 v[0:3], v[4:5], off
	s_nop 0
	global_load_dwordx4 v[4:7], v[4:5], off offset:2048
	s_nop 0
	global_load_dwordx4 v[16:19], v[20:21], off
	s_nop 0
	global_load_dwordx4 v[20:23], v[20:21], off offset:2048
	v_readfirstlane_b32 s9, v32
	s_lshl_b32 s69, s8, 1
	s_lshl_b32 s7, s7, 7
	v_mul_f32_e32 v199, s9, v181
	v_mov_b32_e32 v143, v113
	v_readfirstlane_b32 s10, v199
	s_mov_b32 s6, 0
	s_add_i32 s69, s69, 2
	v_mul_f32_e64 v144, s10, 0
	v_pk_mul_f32 v[146:147], s[10:11], v[116:117] op_sel_hi:[0,1]
	v_pk_mul_f32 v[148:149], s[10:11], v[118:119] op_sel_hi:[0,1]
	v_pk_mul_f32 v[150:151], s[10:11], v[120:121] op_sel_hi:[0,1]
	v_pk_mul_f32 v[152:153], s[10:11], v[122:123] op_sel_hi:[0,1]
	v_pk_mul_f32 v[154:155], s[10:11], v[136:137] op_sel_hi:[0,1]
	v_pk_mul_f32 v[156:157], s[10:11], v[138:139] op_sel_hi:[0,1]
	v_pk_mul_f32 v[158:159], s[10:11], v[140:141] op_sel_hi:[0,1]
	s_or_b32 s70, s67, 15
	v_mov_b32_e32 v145, s10
	s_sub_i32 s71, 0x7ff, s7
	v_mov_b32_e32 v160, 0xff800000
	v_mov_b32_e32 v204, 0
	v_mov_b32_e32 v200, v196
	v_mov_b32_e32 v201, v195
	v_mov_b32_e32 v203, 0
	v_mov_b32_e32 v178, 0xff800000
	s_waitcnt vmcnt(3)
	ds_write_b128 v133, v[0:3]
	s_waitcnt vmcnt(2)
	ds_write_b128 v191, v[4:7] offset:18432
	s_waitcnt vmcnt(1)
	ds_write_b128 v193, v[16:19]
	s_waitcnt vmcnt(0)
; DI unsigned pk2(float lo, float hi) { const f32x2 v = {lo, hi}; return __builtin_bit_cast(unsigned, __builtin_convertvector(v, bf16x2_t)); }
; #define ATT_LOAD(kt_) do { const int k0_ = 64 * (kt_); _Pragma("unroll") for (int i_ = 0; i_ < 2; ++i_) { const int id_ = F.tid + 512 * i_, key_ = id_ >> 4, ch_ = id_ & 15; \
;         st[i_] = *(const u32x4*)(Z + (rowbase + k0_ + key_) * NZ + 4096 + h * 128 + ch_ * 8); st[2 + i_] = *(const u32x4*)(Z + (rowbase + k0_ + key_) * NZ + 5120 + h * 128 + ch_ * 8); } } while (0)
; #define ATT_STORE(s_) do { LAS unsigned char* sb_ = F.lds + (s_) * ATT_STAGE; _Pragma("unroll") for (int i_ = 0; i_ < 2; ++i_) { const int id_ = F.tid + 512 * i_, key_ = id_ >> 4, ch_ = id_ & 15; \
;         *(LAS u32x4*)(sb_ + (ch_ >> 3) * ATT_KMAP + key_ * ATT_KRS + (ch_ & 7) * 16) = st[i_]; *(LAS u32x4*)(sb_ + ATT_VOFF + key_ * ATT_VRS + ch_ * 16) = st[2 + i_]; } } while (0)
; DI void attn_block(const Params& P, const Frame& F, int L, int b, int h, int qb, float lam, float oml) {
;     ...
;         for (int ks = 0; ks < 2; ++ks) { const u32x4 qv = __builtin_bit_cast(u32x4, qf[j][ks]); u32x4 o;
;             o.x = pk2(bflo(qv.x) * sc, bfhi(qv.x) * sc); o.y = pk2(bflo(qv.y) * sc, bfhi(qv.y) * sc); o.z = pk2(bflo(qv.z) * sc, bfhi(qv.z) * sc); o.w = pk2(bflo(qv.w) * sc, bfhi(qv.w) * sc);
;             qf[j][ks] = __builtin_bit_cast(bf16x8, o); }
;     float sbias[16];
; #pragma unroll
;     for (int i = 0; i < 16; ++i) sbias[i] = __builtin_bit_cast(float, __builtin_amdgcn_readfirstlane(__builtin_bit_cast(int, sl * (float)(16 * (i >> 2) + (i & 3)))));
;     f32x4 O[2][8];
; #pragma unroll
;     for (int j = 0; j < 2; ++j)
; #pragma unroll
;         for (int d = 0; d < 8; ++d) O[j][d] = (f32x4){0.f, 0.f, 0.f, 0.f};
;     float mrun[2] = {-INFINITY, -INFINITY}, lrun[2] = {0.f, 0.f};
;     const int nkt = 2 * (qb + 1);
;     u32x4 st[4];
;     ...
;     ATT_LOAD(nkt - 1); ATT_STORE(0); __syncthreads();
; #pragma unroll 1
;     for (int kk = 0; kk < nkt; ++kk) {
;         const int kt = nkt - 1 - kk;
;         if (kk + 1 < nkt) ATT_LOAD(kt - 1);
	ds_write_b128 v194, v[20:23] offset:18432
	v_lshlrev_b32_e32 v32, 16, v8
	v_and_b32_e32 v33, 0xffff0000, v8
	v_lshlrev_b32_e32 v8, 16, v9
	v_and_b32_e32 v9, 0xffff0000, v9
	v_pk_mul_f32 v[32:33], v[32:33], s[56:57] op_sel_hi:[1,0]
	v_pk_mul_f32 v[40:41], v[8:9], s[56:57] op_sel_hi:[1,0]
	v_cvt_pk_bf16_f32 v8, v32, v33
	v_lshlrev_b32_e32 v32, 16, v15
	v_and_b32_e32 v33, 0xffff0000, v15
	v_pk_mul_f32 v[32:33], v[32:33], s[56:57] op_sel_hi:[1,0]
	v_lshlrev_b32_e32 v34, 16, v10
	v_cvt_pk_bf16_f32 v15, v32, v33
	v_lshlrev_b32_e32 v32, 16, v24
	v_and_b32_e32 v33, 0xffff0000, v24
	v_pk_mul_f32 v[32:33], v[32:33], s[56:57] op_sel_hi:[1,0]
	v_and_b32_e32 v35, 0xffff0000, v10
	v_cvt_pk_bf16_f32 v24, v32, v33
	v_lshlrev_b32_e32 v32, 16, v25
	v_and_b32_e32 v33, 0xffff0000, v25
	v_pk_mul_f32 v[32:33], v[32:33], s[56:57] op_sel_hi:[1,0]
	v_lshlrev_b32_e32 v10, 16, v11
	v_cvt_pk_bf16_f32 v25, v32, v33
	v_lshlrev_b32_e32 v32, 16, v26
	v_and_b32_e32 v33, 0xffff0000, v26
	v_pk_mul_f32 v[32:33], v[32:33], s[56:57] op_sel_hi:[1,0]
	v_and_b32_e32 v11, 0xffff0000, v11
	v_cvt_pk_bf16_f32 v26, v32, v33
	v_lshlrev_b32_e32 v32, 16, v27
	v_and_b32_e32 v33, 0xffff0000, v27
	v_pk_mul_f32 v[32:33], v[32:33], s[56:57] op_sel_hi:[1,0]
	v_lshlrev_b32_e32 v36, 16, v12
	v_cvt_pk_bf16_f32 v27, v32, v33
	v_lshlrev_b32_e32 v32, 16, v28
	v_and_b32_e32 v33, 0xffff0000, v28
	v_pk_mul_f32 v[32:33], v[32:33], s[56:57] op_sel_hi:[1,0]
	v_and_b32_e32 v37, 0xffff0000, v12
	v_cvt_pk_bf16_f32 v28, v32, v33
	v_lshlrev_b32_e32 v32, 16, v29
	v_and_b32_e32 v33, 0xffff0000, v29
	v_pk_mul_f32 v[32:33], v[32:33], s[56:57] op_sel_hi:[1,0]
	v_lshlrev_b32_e32 v12, 16, v13
	v_cvt_pk_bf16_f32 v29, v32, v33
	v_lshlrev_b32_e32 v32, 16, v30
	v_and_b32_e32 v33, 0xffff0000, v30
	v_pk_mul_f32 v[32:33], v[32:33], s[56:57] op_sel_hi:[1,0]
	v_and_b32_e32 v13, 0xffff0000, v13
	v_lshlrev_b32_e32 v38, 16, v14
	v_and_b32_e32 v39, 0xffff0000, v14
	v_pk_mul_f32 v[34:35], v[34:35], s[56:57] op_sel_hi:[1,0]
	v_cvt_pk_bf16_f32 v30, v32, v33
	v_lshlrev_b32_e32 v32, 16, v31
	v_and_b32_e32 v33, 0xffff0000, v31
	v_pk_mul_f32 v[42:43], v[10:11], s[56:57] op_sel_hi:[1,0]
	v_pk_mul_f32 v[36:37], v[36:37], s[56:57] op_sel_hi:[1,0]
	v_pk_mul_f32 v[44:45], v[12:13], s[56:57] op_sel_hi:[1,0]
	v_pk_mul_f32 v[38:39], v[38:39], s[56:57] op_sel_hi:[1,0]
	v_cvt_pk_bf16_f32 v10, v34, v35
	v_pk_mul_f32 v[32:33], v[32:33], s[56:57] op_sel_hi:[1,0]
	v_mov_b32_e32 v34, v113
	v_mov_b32_e32 v35, v113
	v_cvt_pk_bf16_f32 v9, v40, v41
	v_cvt_pk_bf16_f32 v11, v42, v43
	v_cvt_pk_bf16_f32 v12, v36, v37
	v_cvt_pk_bf16_f32 v13, v44, v45
	v_cvt_pk_bf16_f32 v14, v38, v39
	v_cvt_pk_bf16_f32 v31, v32, v33
	v_mov_b32_e32 v32, v113
	v_mov_b32_e32 v33, v113
	v_mov_b64_e32 v[42:43], v[34:35]
	v_mov_b64_e32 v[62:63], v[34:35]
	v_mov_b64_e32 v[70:71], v[34:35]
	v_mov_b64_e32 v[46:47], v[34:35]
	v_mov_b64_e32 v[54:55], v[34:35]
	v_mov_b64_e32 v[78:79], v[34:35]
	v_mov_b64_e32 v[90:91], v[34:35]
	v_mov_b64_e32 v[38:39], v[34:35]
	v_mov_b64_e32 v[58:59], v[34:35]
	v_mov_b64_e32 v[82:83], v[34:35]
	v_mov_b64_e32 v[66:67], v[34:35]
	v_mov_b64_e32 v[50:51], v[34:35]
	v_mov_b64_e32 v[74:75], v[34:35]
	v_mov_b64_e32 v[86:87], v[34:35]
	v_mov_b64_e32 v[94:95], v[34:35]
	v_mov_b64_e32 v[40:41], v[32:33]
	v_mov_b64_e32 v[60:61], v[32:33]
	v_mov_b64_e32 v[68:69], v[32:33]
	v_mov_b64_e32 v[44:45], v[32:33]
	v_mov_b64_e32 v[52:53], v[32:33]
	v_mov_b64_e32 v[76:77], v[32:33]
	v_mov_b64_e32 v[88:89], v[32:33]
	v_mov_b64_e32 v[36:37], v[32:33]
	v_mov_b64_e32 v[56:57], v[32:33]
	v_mov_b64_e32 v[80:81], v[32:33]
	v_mov_b64_e32 v[64:65], v[32:33]
	v_mov_b64_e32 v[48:49], v[32:33]
	v_mov_b64_e32 v[72:73], v[32:33]
	v_mov_b64_e32 v[84:85], v[32:33]
	v_mov_b64_e32 v[92:93], v[32:33]
	s_waitcnt lgkmcnt(0)
.Lrot_a_head:
	s_barrier
.LBB0_1054:
	s_add_i32 s72, s6, 1
	s_cmp_lt_u32 s72, s69
	s_cselect_b64 s[60:61], -1, 0
	s_cmp_ge_u32 s72, s69
	s_cbranch_scc1 .LBB0_1056
	s_add_i32 s7, s71, 0xffffff81
	s_ashr_i32 s9, s7, 31
	s_add_u32 s8, s7, s68
	s_addc_u32 s9, s9, 0
	s_waitcnt vmcnt(3)
	v_lshl_add_u64 v[0:1], s[8:9], 0, v[114:115]
	s_waitcnt vmcnt(1)
	v_mov_b64_e32 v[16:17], s[58:59]
	v_mad_u64_u32 v[2:3], s[10:11], v0, s3, v[16:17]
	v_mad_i32_i24 v3, v1, s3, v3
	s_lshl_b32 s38, s66, 1
	v_lshl_add_u64 v[18:19], s[8:9], 0, v[128:129]
	v_lshl_add_u64 v[0:1], v[2:3], 0, s[38:39]
	v_mad_u64_u32 v[16:17], s[8:9], v18, s3, v[16:17]
	v_lshl_add_u64 v[0:1], v[0:1], 0, v[112:113]
	v_mad_i32_i24 v17, v19, s3, v17
	v_add_co_u32_e32 v4, vcc, s33, v0
	v_lshl_add_u64 v[16:17], v[16:17], 0, s[38:39]
	s_nop 0
	v_addc_co_u32_e32 v5, vcc, 0, v1, vcc
	v_lshl_add_u64 v[16:17], v[16:17], 0, v[112:113]
	s_waitcnt vmcnt(0)
	v_add_co_u32_e32 v20, vcc, 0x2000, v16
	global_load_dwordx4 v[0:3], v[4:5], off
	s_nop 0
	global_load_dwordx4 v[4:7], v[4:5], off offset:2048
	v_addc_co_u32_e32 v21, vcc, 0, v17, vcc
	global_load_dwordx4 v[16:19], v[20:21], off
	s_nop 0
	global_load_dwordx4 v[20:23], v[20:21], off offset:2048

; #define ATT_STORE(s_) do { LAS unsigned char* sb_ = F.lds + (s_) * ATT_STAGE; _Pragma("unroll") for (int i_ = 0; i_ < 2; ++i_) { const int id_ = F.tid + 512 * i_, key_ = id_ >> 4, ch_ = id_ & 15; \
;         *(LAS u32x4*)(sb_ + (ch_ >> 3) * ATT_KMAP + key_ * ATT_KRS + (ch_ & 7) * 16) = st[i_]; *(LAS u32x4*)(sb_ + ATT_VOFF + key_ * ATT_VRS + ch_ * 16) = st[2 + i_]; } } while (0)
; DI void attn_block(const Params& P, const Frame& F, int L, int b, int h, int qb, float lam, float oml) {
;     ...
;         if (kk + 1 < nkt) ATT_STORE((kk + 1) & 1);
;         __syncthreads();
;     }
.LBB0_1068:
	s_sub_i32 s71, s71, 64
	v_subrev_u32_e32 v201, 64, v201
	s_cmp_lg_u32 s69, s72
	v_add_u32_e32 v200, 64, v200
	s_waitcnt lgkmcnt(0)
	s_cbranch_scc0 .Lrot_a_exit
	v_mov_b32_e32 v160, v202
	v_mov_b32_e32 v178, v205
	s_mov_b32 s6, s72
	s_branch .Lrot_a_head
.Lrot_a_exit:
	s_barrier
	s_branch .LBB0_1046

; DI unsigned pk2(float lo, float hi) { const f32x2 v = {lo, hi}; return __builtin_bit_cast(unsigned, __builtin_convertvector(v, bf16x2_t)); }
; #define ATT_LOAD(kt_) do { const int k0_ = 64 * (kt_); _Pragma("unroll") for (int i_ = 0; i_ < 2; ++i_) { const int id_ = F.tid + 512 * i_, key_ = id_ >> 4, ch_ = id_ & 15; \
;         st[i_] = *(const u32x4*)(Z + (rowbase + k0_ + key_) * NZ + 4096 + h * 128 + ch_ * 8); st[2 + i_] = *(const u32x4*)(Z + (rowbase + k0_ + key_) * NZ + 5120 + h * 128 + ch_ * 8); } } while (0)
; DI void attn_block(const Params& P, const Frame& F, int L, int b, int h, int qb, float lam, float oml) {
;     ...
;     const int q0 = qb * 128, qrow = q0 + 16 * wave + c;
;     const size_t rowbase = (size_t)b * SEQ;
;     bf16x8 qf[2][2];
; #pragma unroll
;     for (int j = 0; j < 2; ++j)
; #pragma unroll
;         for (int ks = 0; ks < 2; ++ks) qf[j][ks] = *(const bf16x8*)(Z + (rowbase + qrow) * NZ + 3072 + h * 128 + j * 64 + 32 * ks + 8 * rq);
;     const float LOG2E = 1.4426950408889634f;
;     const float sc = 0.125f * LOG2E, sl = __builtin_bit_cast(float, __builtin_amdgcn_readfirstlane(__builtin_bit_cast(int, exp2f(-(float)(h + 1)) * LOG2E)));
; #pragma unroll
;     for (int j = 0; j < 2; ++j)
; #pragma unroll
;         for (int ks = 0; ks < 2; ++ks) { const u32x4 qv = __builtin_bit_cast(u32x4, qf[j][ks]); u32x4 o;
;             o.x = pk2(bflo(qv.x) * sc, bfhi(qv.x) * sc); o.y = pk2(bflo(qv.y) * sc, bfhi(qv.y) * sc); o.z = pk2(bflo(qv.z) * sc, bfhi(qv.z) * sc); o.w = pk2(bflo(qv.w) * sc, bfhi(qv.w) * sc);
;             qf[j][ks] = __builtin_bit_cast(bf16x8, o); }
;     float sbias[16];
; #pragma unroll
;     for (int i = 0; i < 16; ++i) sbias[i] = __builtin_bit_cast(float, __builtin_amdgcn_readfirstlane(__builtin_bit_cast(int, sl * (float)(16 * (i >> 2) + (i & 3)))));
;     f32x4 O[2][8];
; #pragma unroll
;     for (int j = 0; j < 2; ++j)
; #pragma unroll
;         for (int d = 0; d < 8; ++d) O[j][d] = (f32x4){0.f, 0.f, 0.f, 0.f};
;     float mrun[2] = {-INFINITY, -INFINITY}, lrun[2] = {0.f, 0.f};
;     const int nkt = 2 * (qb + 1);
;     u32x4 st[4];
;     ...
;     ATT_LOAD(nkt - 1); ATT_STORE(0); __syncthreads();
.LBB0_2617:
	s_or_b64 exec, exec, s[6:7]
	v_mov_b32_e32 v0, s67
	s_waitcnt lgkmcnt(0)
	s_barrier
	ds_read_b32 v0, v0
	s_mov_b64 s[6:7], -1
	s_waitcnt lgkmcnt(0)
	v_cmp_lt_i32_e32 vcc, s3, v0
	v_readfirstlane_b32 s10, v0
	s_cbranch_vccnz .LBB0_2612
	s_ashr_i32 s7, s10, 6
	s_sub_i32 s8, 15, s7
	s_lshl_b32 s9, s8, 7
	s_add_i32 s69, s9, s66
	s_lshl_b32 s6, s10, 8
	v_or_b32_e32 v0, s69, v103
	s_and_b32 s70, s6, 0x3800
	s_and_b32 s12, s10, 7
	v_add_u32_e32 v126, s70, v0
	v_mov_b64_e32 v[0:1], s[56:57]
	v_mad_u64_u32 v[2:3], s[10:11], v126, s33, v[0:1]
	s_lshl_b32 s40, s12, 8
	v_lshl_add_u64 v[2:3], v[2:3], 0, s[40:41]
	v_lshl_add_u64 v[2:3], v[100:101], 1, v[2:3]
	v_add_co_u32_e32 v4, vcc, s47, v2
	s_lshl_b32 s68, s12, 7
	s_nop 0
	v_addc_co_u32_e32 v5, vcc, 0, v3, vcc
	global_load_dwordx4 v[8:11], v[4:5], off offset:2048
	v_lshl_add_u64 v[2:3], v[2:3], 0, s[42:43]
	global_load_dwordx4 v[12:15], v[2:3], off offset:64
	global_load_dwordx4 v[16:19], v[2:3], off offset:128
	s_add_i32 s12, s12, 1
	v_cvt_f32_ubyte0_e32 v4, s12
	v_cmp_lt_f32_e32 vcc, s62, v4
	s_and_b64 s[12:13], vcc, exec
	s_cselect_b32 s12, 0xffffffc0, 0
	s_add_i32 s9, s70, s9
	s_mov_b32 s11, s41
	v_cndmask_b32_e32 v5, 0, v180, vcc
	global_load_dwordx4 v[28:31], v[2:3], off offset:192
	s_or_b32 s10, s9, 64
	v_sub_f32_e32 v4, v5, v4
	v_lshl_add_u64 v[2:3], s[10:11], 0, v[98:99]
	v_exp_f32_e32 v20, v4
	v_lshl_add_u64 v[4:5], s[10:11], 0, v[104:105]
	v_mad_u64_u32 v[6:7], s[10:11], v2, s33, v[0:1]
	v_mad_i32_i24 v7, v3, s33, v7
	v_lshlrev_b32_e32 v96, 1, v102
	v_mad_u64_u32 v[0:1], s[10:11], v4, s33, v[0:1]
	v_lshl_add_u64 v[2:3], v[6:7], 0, s[40:41]
	v_mad_i32_i24 v1, v5, s33, v1
	v_lshl_add_u64 v[2:3], v[2:3], 0, v[96:97]
	v_lshl_add_u64 v[0:1], v[0:1], 0, s[40:41]
	v_add_co_u32_e32 v4, vcc, s63, v2
	v_lshl_add_u64 v[0:1], v[0:1], 0, v[96:97]
	s_nop 0
	v_addc_co_u32_e32 v5, vcc, 0, v3, vcc
	v_add_co_u32_e32 v24, vcc, s63, v0
	v_ldexp_f32 v32, v20, s12
	s_nop 0
	v_addc_co_u32_e32 v25, vcc, 0, v1, vcc
	global_load_dwordx4 v[0:3], v[4:5], off
	s_nop 0
	global_load_dwordx4 v[4:7], v[4:5], off offset:2048
	s_nop 0
	global_load_dwordx4 v[20:23], v[24:25], off
	s_nop 0
	global_load_dwordx4 v[24:27], v[24:25], off offset:2048
	v_readfirstlane_b32 s9, v32
	s_lshl_b32 s71, s8, 1
	s_lshl_b32 s7, s7, 7
	v_mul_f32_e32 v199, s9, v181
	v_mov_b32_e32 v127, v97
	v_readfirstlane_b32 s10, v199
	s_mov_b32 s6, 0
	s_add_i32 s71, s71, 2
	v_mul_f32_e64 v128, s10, 0
	v_pk_mul_f32 v[130:131], s[10:11], v[112:113] op_sel_hi:[0,1]
	v_pk_mul_f32 v[132:133], s[10:11], v[114:115] op_sel_hi:[0,1]
	v_pk_mul_f32 v[134:135], s[10:11], v[116:117] op_sel_hi:[0,1]
	v_pk_mul_f32 v[136:137], s[10:11], v[118:119] op_sel_hi:[0,1]
	v_pk_mul_f32 v[138:139], s[10:11], v[120:121] op_sel_hi:[0,1]
	v_pk_mul_f32 v[140:141], s[10:11], v[122:123] op_sel_hi:[0,1]
	v_pk_mul_f32 v[142:143], s[10:11], v[124:125] op_sel_hi:[0,1]
	s_or_b32 s72, s69, 15
	v_mov_b32_e32 v129, s10
	s_sub_i32 s73, 0x7ff, s7
	v_mov_b32_e32 v144, 0xff800000
	v_mov_b32_e32 v203, 0
	v_mov_b32_e32 v200, v196
	v_mov_b32_e32 v201, v195
	v_mov_b32_e32 v202, 0
	v_mov_b32_e32 v162, 0xff800000
	s_waitcnt vmcnt(3)
	ds_write_b128 v109, v[0:3]
	s_waitcnt vmcnt(2)
	ds_write_b128 v191, v[4:7] offset:18432
	s_waitcnt vmcnt(1)
	ds_write_b128 v193, v[20:23]
	s_waitcnt vmcnt(0)
	ds_write_b128 v194, v[24:27] offset:18432
	v_lshlrev_b32_e32 v32, 16, v8
	v_and_b32_e32 v33, 0xffff0000, v8
	v_lshlrev_b32_e32 v8, 16, v9
	v_and_b32_e32 v9, 0xffff0000, v9
	v_pk_mul_f32 v[32:33], v[32:33], s[46:47] op_sel_hi:[1,0]
	v_pk_mul_f32 v[40:41], v[8:9], s[46:47] op_sel_hi:[1,0]
	v_cvt_pk_bf16_f32 v8, v32, v33
	v_lshlrev_b32_e32 v32, 16, v15
	v_and_b32_e32 v33, 0xffff0000, v15
	v_pk_mul_f32 v[32:33], v[32:33], s[46:47] op_sel_hi:[1,0]
	v_lshlrev_b32_e32 v34, 16, v10
	v_cvt_pk_bf16_f32 v15, v32, v33
	v_lshlrev_b32_e32 v32, 16, v16
	v_and_b32_e32 v33, 0xffff0000, v16
	v_pk_mul_f32 v[32:33], v[32:33], s[46:47] op_sel_hi:[1,0]
	v_and_b32_e32 v35, 0xffff0000, v10
	v_cvt_pk_bf16_f32 v16, v32, v33
	v_lshlrev_b32_e32 v32, 16, v17
	v_and_b32_e32 v33, 0xffff0000, v17
	v_pk_mul_f32 v[32:33], v[32:33], s[46:47] op_sel_hi:[1,0]
	v_lshlrev_b32_e32 v10, 16, v11
	v_cvt_pk_bf16_f32 v17, v32, v33
	v_lshlrev_b32_e32 v32, 16, v18
	v_and_b32_e32 v33, 0xffff0000, v18
	v_pk_mul_f32 v[32:33], v[32:33], s[46:47] op_sel_hi:[1,0]
	v_and_b32_e32 v11, 0xffff0000, v11
	v_cvt_pk_bf16_f32 v18, v32, v33
	v_lshlrev_b32_e32 v32, 16, v19
	v_and_b32_e32 v33, 0xffff0000, v19
	v_pk_mul_f32 v[32:33], v[32:33], s[46:47] op_sel_hi:[1,0]
	v_lshlrev_b32_e32 v36, 16, v12
	v_cvt_pk_bf16_f32 v19, v32, v33
	v_lshlrev_b32_e32 v32, 16, v28
	v_and_b32_e32 v33, 0xffff0000, v28
	v_pk_mul_f32 v[32:33], v[32:33], s[46:47] op_sel_hi:[1,0]
	v_and_b32_e32 v37, 0xffff0000, v12
	v_cvt_pk_bf16_f32 v28, v32, v33
	v_lshlrev_b32_e32 v32, 16, v29
	v_and_b32_e32 v33, 0xffff0000, v29
	v_pk_mul_f32 v[32:33], v[32:33], s[46:47] op_sel_hi:[1,0]
	v_lshlrev_b32_e32 v12, 16, v13
	v_cvt_pk_bf16_f32 v29, v32, v33
	v_lshlrev_b32_e32 v32, 16, v30
	v_and_b32_e32 v33, 0xffff0000, v30
	v_pk_mul_f32 v[32:33], v[32:33], s[46:47] op_sel_hi:[1,0]
	v_and_b32_e32 v13, 0xffff0000, v13
	v_lshlrev_b32_e32 v38, 16, v14
	v_and_b32_e32 v39, 0xffff0000, v14
	v_pk_mul_f32 v[34:35], v[34:35], s[46:47] op_sel_hi:[1,0]
	v_cvt_pk_bf16_f32 v30, v32, v33
	v_lshlrev_b32_e32 v32, 16, v31
	v_and_b32_e32 v33, 0xffff0000, v31
	v_pk_mul_f32 v[42:43], v[10:11], s[46:47] op_sel_hi:[1,0]
	v_pk_mul_f32 v[36:37], v[36:37], s[46:47] op_sel_hi:[1,0]
	v_pk_mul_f32 v[44:45], v[12:13], s[46:47] op_sel_hi:[1,0]
	v_pk_mul_f32 v[38:39], v[38:39], s[46:47] op_sel_hi:[1,0]
	v_cvt_pk_bf16_f32 v10, v34, v35
	v_pk_mul_f32 v[32:33], v[32:33], s[46:47] op_sel_hi:[1,0]
	v_mov_b32_e32 v34, v97
	v_mov_b32_e32 v35, v97
	v_cvt_pk_bf16_f32 v9, v40, v41
	v_cvt_pk_bf16_f32 v11, v42, v43
	v_cvt_pk_bf16_f32 v12, v36, v37
	v_cvt_pk_bf16_f32 v13, v44, v45
	v_cvt_pk_bf16_f32 v14, v38, v39
	v_cvt_pk_bf16_f32 v31, v32, v33
	v_mov_b32_e32 v32, v97
	v_mov_b32_e32 v33, v97
	v_mov_b64_e32 v[42:43], v[34:35]
	v_mov_b64_e32 v[50:51], v[34:35]
	v_mov_b64_e32 v[54:55], v[34:35]
	v_mov_b64_e32 v[62:63], v[34:35]
	v_mov_b64_e32 v[74:75], v[34:35]
	v_mov_b64_e32 v[82:83], v[34:35]
	v_mov_b64_e32 v[90:91], v[34:35]
	v_mov_b64_e32 v[38:39], v[34:35]
	v_mov_b64_e32 v[46:47], v[34:35]
	v_mov_b64_e32 v[58:59], v[34:35]
	v_mov_b64_e32 v[66:67], v[34:35]
	v_mov_b64_e32 v[70:71], v[34:35]
	v_mov_b64_e32 v[78:79], v[34:35]
	v_mov_b64_e32 v[86:87], v[34:35]
	v_mov_b64_e32 v[94:95], v[34:35]
	v_mov_b64_e32 v[40:41], v[32:33]
	v_mov_b64_e32 v[48:49], v[32:33]
	v_mov_b64_e32 v[52:53], v[32:33]
	v_mov_b64_e32 v[60:61], v[32:33]
	v_mov_b64_e32 v[72:73], v[32:33]
	v_mov_b64_e32 v[80:81], v[32:33]
	v_mov_b64_e32 v[88:89], v[32:33]
	v_mov_b64_e32 v[36:37], v[32:33]
	v_mov_b64_e32 v[44:45], v[32:33]
	v_mov_b64_e32 v[56:57], v[32:33]
	v_mov_b64_e32 v[64:65], v[32:33]
	v_mov_b64_e32 v[68:69], v[32:33]
	v_mov_b64_e32 v[76:77], v[32:33]
	v_mov_b64_e32 v[84:85], v[32:33]
	v_mov_b64_e32 v[92:93], v[32:33]
	s_waitcnt lgkmcnt(0)
; #define ATT_LOAD(kt_) do { const int k0_ = 64 * (kt_); _Pragma("unroll") for (int i_ = 0; i_ < 2; ++i_) { const int id_ = F.tid + 512 * i_, key_ = id_ >> 4, ch_ = id_ & 15; \
;         st[i_] = *(const u32x4*)(Z + (rowbase + k0_ + key_) * NZ + 4096 + h * 128 + ch_ * 8); st[2 + i_] = *(const u32x4*)(Z + (rowbase + k0_ + key_) * NZ + 5120 + h * 128 + ch_ * 8); } } while (0)
; #define ATT_STORE(s_) do { LAS unsigned char* sb_ = F.lds + (s_) * ATT_STAGE; _Pragma("unroll") for (int i_ = 0; i_ < 2; ++i_) { const int id_ = F.tid + 512 * i_, key_ = id_ >> 4, ch_ = id_ & 15; \
;         *(LAS u32x4*)(sb_ + (ch_ >> 3) * ATT_KMAP + key_ * ATT_KRS + (ch_ & 7) * 16) = st[i_]; *(LAS u32x4*)(sb_ + ATT_VOFF + key_ * ATT_VRS + ch_ * 16) = st[2 + i_]; } } while (0)
; DI void attn_block(const Params& P, const Frame& F, int L, int b, int h, int qb, float lam, float oml) {
;     ...
;     ATT_LOAD(nkt - 1); ATT_STORE(0); __syncthreads();
; #pragma unroll 1
;     for (int kk = 0; kk < nkt; ++kk) {
;         const int kt = nkt - 1 - kk;
;         if (kk + 1 < nkt) ATT_LOAD(kt - 1);
.Lrot_b_head:
	s_barrier
.LBB0_2619:
	s_add_i32 s74, s6, 1
	s_cmp_lt_u32 s74, s71
	s_cselect_b64 s[58:59], -1, 0
	s_cmp_ge_u32 s74, s71
	s_cbranch_scc1 .LBB0_2621
	s_add_i32 s7, s73, 0xffffff81
	s_ashr_i32 s9, s7, 31
	s_add_u32 s8, s7, s70
	s_addc_u32 s9, s9, 0
	s_waitcnt vmcnt(3)
	v_lshl_add_u64 v[0:1], s[8:9], 0, v[98:99]
	s_waitcnt vmcnt(1)
	v_mov_b64_e32 v[20:21], s[56:57]
	v_mad_u64_u32 v[2:3], s[10:11], v0, s33, v[20:21]
	v_mad_i32_i24 v3, v1, s33, v3
	s_lshl_b32 s40, s68, 1
	v_lshl_add_u64 v[22:23], s[8:9], 0, v[104:105]
	v_lshl_add_u64 v[0:1], v[2:3], 0, s[40:41]
	v_mad_u64_u32 v[20:21], s[8:9], v22, s33, v[20:21]
	v_lshl_add_u64 v[0:1], v[0:1], 0, v[96:97]
	v_mad_i32_i24 v21, v23, s33, v21
	v_add_co_u32_e32 v4, vcc, s63, v0
	v_lshl_add_u64 v[20:21], v[20:21], 0, s[40:41]
	s_nop 0
	v_addc_co_u32_e32 v5, vcc, 0, v1, vcc
	v_lshl_add_u64 v[20:21], v[20:21], 0, v[96:97]
	s_waitcnt vmcnt(0)
	v_add_co_u32_e32 v24, vcc, 0x2000, v20
	global_load_dwordx4 v[0:3], v[4:5], off
	s_nop 0
	global_load_dwordx4 v[4:7], v[4:5], off offset:2048
	v_addc_co_u32_e32 v25, vcc, 0, v21, vcc
	global_load_dwordx4 v[20:23], v[24:25], off
	s_nop 0
	global_load_dwordx4 v[24:27], v[24:25], off offset:2048

; #define ATT_STORE(s_) do { LAS unsigned char* sb_ = F.lds + (s_) * ATT_STAGE; _Pragma("unroll") for (int i_ = 0; i_ < 2; ++i_) { const int id_ = F.tid + 512 * i_, key_ = id_ >> 4, ch_ = id_ & 15; \
;         *(LAS u32x4*)(sb_ + (ch_ >> 3) * ATT_KMAP + key_ * ATT_KRS + (ch_ & 7) * 16) = st[i_]; *(LAS u32x4*)(sb_ + ATT_VOFF + key_ * ATT_VRS + ch_ * 16) = st[2 + i_]; } } while (0)
; DI void attn_block(const Params& P, const Frame& F, int L, int b, int h, int qb, float lam, float oml) {
;     ...
;         if (kk + 1 < nkt) ATT_STORE((kk + 1) & 1);
;         __syncthreads();
;     }
.LBB0_2633:
	s_sub_i32 s73, s73, 64
	v_subrev_u32_e32 v201, 64, v201
	s_cmp_lg_u32 s71, s74
	v_add_u32_e32 v200, 64, v200
	s_waitcnt lgkmcnt(0)
	s_cbranch_scc0 .Lrot_b_exit
	v_mov_b32_e32 v144, v204
	v_mov_b32_e32 v162, v205
	s_mov_b32 s6, s74
	s_branch .Lrot_b_head
